# in-proj and out-proj GEMM phases walk their unit lists in reverse order (most recently written operand panels first), on top of nt loads + reversed P6
# speedup vs baseline: 1.0031x; 1.0031x over previous
; #define LAS __attribute__((address_space(3)))
; __device__ __forceinline__ int fresh_lane() { unsigned z = 0u; asm volatile("" : "+v"(z)); return (int)__builtin_amdgcn_mbcnt_hi(~0u, __builtin_amdgcn_mbcnt_lo(~0u, z)); }
;     __device__ __forceinline__ bool next(int i, Unit& u) const {
;         const long L = (long)i * G + c; if (L >= nwg) return false;
;         int wgid = (int)L; { const int q = nwg / NXCD, r = nwg % NXCD, xcd = wgid % NXCD, off = wgid / NXCD; wgid = (xcd < r ? xcd * (q + 1) : r * (q + 1) + (xcd - r) * q) + off; }
;         const int nig = WGM * nN, gid = wgid / nig, fm = gid * WGM, gsz = (nM - fm) < WGM ? (nM - fm) : WGM;
;         u.pm = fm + ((wgid % nig) % gsz); u.pn = (wgid % nig) / gsz; u.e = 0; u.pos0 = 0; u.cnt = 0; return true;
; __device__ __forceinline__ void ph1(const Ctx& c) {
;     const P& p = *c.pp;
;     pg8::RowOrder S; S.init(T, INW, c.G, c.bx, p.ws + WS_MIXED, p.ws + WS_WIN);
;     pg8::EpiQKV E{c.pp};
;     { const int t = c.wave * 64 + fresh_lane(); LAS float* tab = (LAS float*)(c.lds + TAB_EPI);
;       if (t < 336) tab[t] = t < 64 ? p.g_q_swa[t] : t < 128 ? p.g_k_swa[t - 64] : t < 160 ? p.g_q_diff[t - 128] : t < 192 ? p.g_k_diff[t - 160] : ((const float*)(p.ws + WS_ROT))[t - 192];
;       __syncthreads(); }
;     pg8::gemm_phase<pg8::EpiQKV, pg8::RowOrder>(c.lds + RING_OFF, S, E, c.wave);
.LBB7_208:
	s_or_b64 exec, exec, s[0:1]
	s_cmpk_lt_i32 s92, 0x900
	v_mov_b32_e32 v0, 0
	s_cselect_b64 s[0:1], -1, 0
	s_cmpk_gt_i32 s92, 0x8ff
	s_waitcnt lgkmcnt(0)
	s_barrier
	s_cbranch_scc1 .LBB7_210
	s_sub_i32 s100, 0x8ff, s92
	s_ashr_i32 s2, s100, 31
	s_lshr_b32 s2, s2, 29
	s_add_i32 s2, s100, s2
	s_ashr_i32 s4, s2, 3
	s_and_b32 s2, s2, -8
	s_sub_i32 s2, s100, s2
	s_cmp_lt_i32 s2, 0
	s_movk_i32 s5, 0x121
	s_cselect_b32 s5, s5, 0x120
	s_mul_i32 s2, s5, s2
	s_add_i32 s2, s2, s4
	s_mul_hi_i32 s4, s2, 0x38e38e39
	s_lshr_b32 s5, s4, 31
	s_ashr_i32 s4, s4, 4
	s_add_i32 s4, s4, s5
	s_lshl_b32 s5, s4, 3
	s_mulk_i32 s4, 0x48
	s_sub_i32 s2, s2, s4
	s_bfe_i32 s4, s2, 0x80000
	s_bfe_u32 s4, s4, 0x3000c
	s_add_i32 s4, s2, s4
	s_bfe_i32 s8, s4, 0x80000
	s_and_b32 s4, s4, 0xf8
	s_sub_i32 s2, s2, s4
	s_sext_i32_i16 s8, s8
	s_sext_i32_i8 s2, s2
	s_add_i32 s4, s5, s2
	s_ashr_i32 s8, s8, 3

;     __device__ __forceinline__ bool next(int i, Unit& u) const {
;         const long L = (long)i * G + c; if (L >= nwg) return false;
;         int wgid = (int)L; { const int q = nwg / NXCD, r = nwg % NXCD, xcd = wgid % NXCD, off = wgid / NXCD; wgid = (xcd < r ? xcd * (q + 1) : r * (q + 1) + (xcd - r) * q) + off; }
;         const int nig = WGM * nN, gid = wgid / nig, fm = gid * WGM, gsz = (nM - fm) < WGM ? (nM - fm) : WGM;
;         u.pm = fm + ((wgid % nig) % gsz); u.pn = (wgid % nig) / gsz; u.e = 0; u.pos0 = 0; u.cnt = 0; return true;
; template <class Epi, class Sched>
; __device__ __forceinline__ void gemm_phase(LAS unsigned char* lds, const Sched& S, const Epi& E, const int wid) {
;     ...
;         const bool has_next = S.next(ui + 1, nxt);
;         const char* nA = has_next ? S.aptr(nxt) : cA; const char* nB = has_next ? S.bptr(nxt) : cB;
.LBB7_216:
	s_add_i32 s73, s73, 1
	s_mul_i32 s0, s73, s70
	s_mul_hi_u32 s1, s73, s3
	s_add_i32 s1, s1, s0
	s_mul_i32 s0, s73, s3
	s_add_u32 s40, s0, s92
	s_addc_u32 s41, s1, s71
	v_cmp_gt_i64_e32 vcc, s[40:41], v[170:171]
	v_cmp_lt_i64_e64 s[0:1], s[40:41], v[168:169]
	s_cbranch_vccnz .LBB7_218
	s_sub_i32 s40, 0x8ff, s40
	s_ashr_i32 s5, s40, 31
	s_lshr_b32 s5, s5, 29
	s_add_i32 s5, s40, s5
	s_ashr_i32 s16, s5, 3
	s_and_b32 s5, s5, -8
	s_sub_i32 s5, s40, s5
	s_cmp_lt_i32 s5, 0
	s_movk_i32 s17, 0x121
	s_cselect_b32 s17, s17, 0x120
	s_mul_i32 s5, s17, s5
	s_add_i32 s5, s5, s16
	s_mul_hi_i32 s16, s5, 0x38e38e39
	s_lshr_b32 s17, s16, 31
	s_ashr_i32 s16, s16, 4
	s_add_i32 s16, s16, s17
	s_lshl_b32 s17, s16, 3
	s_sub_i32 s36, 0x100, s17
	s_min_i32 s36, s36, 8
	s_abs_i32 s37, s36
	v_cvt_f32_u32_e32 v0, s37
	s_sub_i32 s39, 0, s37
	s_mulk_i32 s16, 0x48
	s_sub_i32 s5, s5, s16
	v_rcp_iflag_f32_e32 v0, v0
	s_abs_i32 s16, s5
	s_xor_b32 s38, s5, s36
	s_ashr_i32 s38, s38, 31
	v_mul_f32_e32 v0, 0x4f7ffffe, v0
	v_cvt_u32_f32_e32 v0, v0
	s_nop 0
	v_readfirstlane_b32 s40, v0
	s_mul_i32 s39, s39, s40
	s_mul_hi_u32 s39, s40, s39
	s_add_i32 s40, s40, s39
	s_mul_hi_u32 s39, s16, s40
	s_mul_i32 s40, s39, s37
	s_sub_i32 s16, s16, s40
	s_add_i32 s41, s39, 1
	s_sub_i32 s40, s16, s37
	s_cmp_ge_u32 s16, s37
	s_cselect_b32 s39, s41, s39
	s_cselect_b32 s16, s40, s16
	s_add_i32 s40, s39, 1
	s_cmp_ge_u32 s16, s37
	s_cselect_b32 s16, s40, s39
	s_xor_b32 s16, s16, s38
	s_sub_i32 s16, s16, s38
	s_mul_i32 s36, s16, s36
	s_sub_i32 s5, s5, s36
	s_add_i32 s38, s5, s17

;     __device__ __forceinline__ bool next(int i, Unit& u) const {
;         const long L = (long)i * G + c; if (L >= nwg) return false;
;         int wgid = (int)L; { const int q = nwg / NXCD, r = nwg % NXCD, xcd = wgid % NXCD, off = wgid / NXCD; wgid = (xcd < r ? xcd * (q + 1) : r * (q + 1) + (xcd - r) * q) + off; }
;         const int nig = WGM * nN, gid = wgid / nig, fm = gid * WGM, gsz = (nM - fm) < WGM ? (nM - fm) : WGM;
;         u.pm = fm + ((wgid % nig) % gsz); u.pn = (wgid % nig) / gsz; u.e = 0; u.pos0 = 0; u.cnt = 0; return true;
; __device__ __forceinline__ void ph3(const Ctx& c) {
;     const P& p = *c.pp;
;     pg8::RowOrder S; S.init(T, DM, c.G, c.bx, p.ws + WS_MIXED, p.ws + WS_WOUT);
;     pg8::EpiO E{(bf16_t*)p.out};
;     pg8::gemm_phase<pg8::EpiO, pg8::RowOrder>(c.lds + RING_OFF, S, E, c.wave);
.LBB7_609:
	v_readlane_b32 s4, v254, 2
	v_readlane_b32 s5, v254, 3
	s_cmp_lt_i32 s4, 4
	s_cselect_b64 s[4:5], -1, 0
	s_and_b64 s[0:1], s[4:5], s[0:1]
	s_andn2_b64 vcc, exec, s[0:1]
	s_cbranch_vccnz .LBB7_634
	s_waitcnt vmcnt(0)
	v_mov_b32_e32 v0, 0
	s_cmpk_gt_i32 s92, 0x3ff
	s_cbranch_scc1 .LBB7_634
	s_ashr_i32 s2, s92, 31
	s_lshr_b32 s0, s2, 29
	s_sub_i32 s100, 0x3ff, s92
	s_add_i32 s8, s100, s0
	s_and_b32 s0, s8, -8
	s_sub_i32 s7, s100, s0
	s_cmp_gt_i32 s7, -1
	s_cbranch_scc0 .LBB7_613
	s_lshl_b32 s6, s7, 7
	s_ashr_i32 s0, s8, 3
	s_cbranch_execz .LBB7_614
	s_branch .LBB7_615

;     __device__ __forceinline__ bool next(int i, Unit& u) const {
;         const long L = (long)i * G + c; if (L >= nwg) return false;
;         int wgid = (int)L; { const int q = nwg / NXCD, r = nwg % NXCD, xcd = wgid % NXCD, off = wgid / NXCD; wgid = (xcd < r ? xcd * (q + 1) : r * (q + 1) + (xcd - r) * q) + off; }
;         const int nig = WGM * nN, gid = wgid / nig, fm = gid * WGM, gsz = (nM - fm) < WGM ? (nM - fm) : WGM;
;         u.pm = fm + ((wgid % nig) % gsz); u.pn = (wgid % nig) / gsz; u.e = 0; u.pos0 = 0; u.cnt = 0; return true;
; template <class Epi, class Sched>
; __device__ __forceinline__ void gemm_phase(LAS unsigned char* lds, const Sched& S, const Epi& E, const int wid) {
;     ...
;         const bool has_next = S.next(ui + 1, nxt);
;         const char* nA = has_next ? S.aptr(nxt) : cA; const char* nB = has_next ? S.bptr(nxt) : cB;
.LBB7_620:
	s_add_i32 s35, s35, 1
	s_mul_i32 s0, s35, s71
	s_mul_hi_u32 s1, s35, s3
	s_add_i32 s1, s1, s0
	s_mul_i32 s0, s35, s3
	s_add_u32 s40, s0, s92
	s_addc_u32 s41, s1, s2
	v_cmp_gt_i64_e32 vcc, s[40:41], v[130:131]
	v_cmp_lt_i64_e64 s[0:1], s[40:41], v[128:129]
	s_cbranch_vccnz .LBB7_626
	s_sub_i32 s40, 0x3ff, s40
	s_ashr_i32 s24, s40, 31
	s_lshr_b32 s24, s24, 29
	s_add_i32 s38, s40, s24
	s_and_b32 s24, s38, -8
	s_sub_i32 s39, s40, s24
	s_cmp_gt_i32 s39, -1
	s_mov_b64 s[24:25], -1
	s_cbranch_scc0 .LBB7_623
	s_lshl_b32 s40, s39, 7
	s_mov_b64 s[24:25], 0
